# P7,P8: the half-workgroup alignment barrier moved behind the first epilogue block so the leading half's epilogue overlaps the lagging half's last MFMA segment
# baseline (speedup 1.0000x reference)
; __device__ __forceinline__ unsigned pk4_fp8(float a, float b, float c, float d) { int v = 0; v = __builtin_amdgcn_cvt_pk_fp8_f32(a, b, v, false); v = __builtin_amdgcn_cvt_pk_fp8_f32(c, d, v, true); return (unsigned)v; }
;     __device__ __forceinline__ void operator()(const f32x4 (&acc)[2][2][4][2], const pg8::Unit& u, const Pre& q, int wr, int wc, int fr, int fq) const {
;         const int row0 = u.pm * 256 + wr * 64 + fr, f0w = u.pn * 128 + wc * 32;
;         constexpr float DS = 1.0f / (FP8_SA * FP8_SW);
;         f32x4 dsk = (f32x4){DS * KP, DS * KP, DS * KP, DS * KP}, dsu = (f32x4){DS, DS, DS, DS}; asm volatile("" : "+v"(dsk), "+v"(dsu));
; #pragma unroll
;         for (int ai = 0; ai < 2; ++ai)
; #pragma unroll
;             for (int mp = 0; mp < 2; ++mp) { unsigned lo[2], hi[2];
; #pragma unroll
;                 for (int mm = 0; mm < 2; ++mm) { const int m = 2 * mp + mm; float h[8];
; #pragma unroll
;                     for (int n = 0; n < 2; ++n) { const f32x4 gk = __builtin_elementwise_fma(acc[ai][0][m][n], dsk, q.bg[n]), up = __builtin_elementwise_fma(acc[ai][1][m][n], dsu, q.bu[n]);
; #pragma unroll
;                         for (int j = 0; j < 4; ++j) { const float gm = __builtin_fmaxf(gk[j], 7.0f * KP), li = __builtin_amdgcn_fmed3f(up[j], -7.0f, 7.0f);
;                             const float sg = __builtin_amdgcn_rcpf(1.0f + __builtin_amdgcn_exp2f(gm));
;                             h[n * 4 + j] = (gm * sg) * (li * (FP8_SH / KP) + (FP8_SH / KP)); } }
;                     lo[mm] = pk4_fp8(h[0], h[1], h[2], h[3]); hi[mm] = pk4_fp8(h[4], h[5], h[6], h[7]); }
;                 const v2u r0 = __builtin_amdgcn_permlane16_swap(lo[0], lo[1], false, false), r1 = __builtin_amdgcn_permlane16_swap(hi[0], hi[1], false, false);
;                 unsigned char* rowp = hb + (size_t)(row0 + ai * 128 + (2 * mp + (fq & 1)) * 16) * FF + f0w + 16 * (fq >> 1);
;                 *(v4u*)rowp = (v4u){r0.x, r1.x, r0.y, r1.y}; }
;     }
.LBB0_739:
	v_mov_b32_e32 v11, v0
	v_mov_b32_e32 v43, v42
	v_readfirstlane_b32 s19, v11
	v_mov_b32_e32 v47, v46
	s_ashr_i32 s27, s19, 2
	v_mov_b32_e32 v44, v42
	v_mov_b32_e32 v45, v42
	v_mov_b32_e32 v48, v46
	v_mov_b32_e32 v49, v46
	v_mov_b64_e32 v[2:3], v[46:47]
	v_mov_b64_e32 v[6:7], v[42:43]
	v_pk_mul_f32 v[18:19], v[78:79], s[16:17] op_sel_hi:[1,0]
	s_lshl_b32 s21, s38, 8
	s_andn2_b32 s27, s27, 63
	v_mov_b64_e32 v[4:5], v[48:49]
	v_mov_b64_e32 v[8:9], v[44:45]
	s_add_i32 s27, s27, s21
	v_and_or_b32 v10, v11, 31, s27
	v_pk_fma_f32 v[20:21], v[178:179], v[6:7], v[18:19]
	v_lshrrev_b32_e32 v11, 1, v11
	v_max_f32_e32 v23, 0xc1898193, v20
	v_and_b32_e32 v186, 16, v11
	v_exp_f32_e32 v11, v23
	v_max_f32_e32 v21, 0xc1898193, v21
	v_pk_fma_f32 v[28:29], v[182:183], v[2:3], v[38:39]
	v_pk_mul_f32 v[16:17], v[80:81], s[16:17] op_sel_hi:[1,0]
	v_add_f32_e32 v11, 1.0, v11
	v_rcp_f32_e32 v189, v11
	v_exp_f32_e32 v11, v21
	v_med3_f32 v22, v28, s94, v202
	v_pk_fma_f32 v[24:25], v[180:181], v[8:9], v[16:17]
	v_pk_mul_f32 v[22:23], v[22:23], v[188:189]
	v_add_f32_e32 v11, 1.0, v11
	v_sub_f32_e32 v20, 0xbfd083aa, v22
	v_mul_f32_e32 v30, v20, v23
	v_max_f32_e32 v23, 0xc1898193, v24
	v_rcp_f32_e32 v189, v11
	v_exp_f32_e32 v11, v23
	v_med3_f32 v20, v29, s94, v202
	v_max_f32_e32 v25, 0xc1898193, v25
	v_pk_mul_f32 v[20:21], v[20:21], v[188:189]
	v_add_f32_e32 v11, 1.0, v11
	v_rcp_f32_e32 v189, v11
	v_exp_f32_e32 v11, v25
	v_pk_fma_f32 v[26:27], v[184:185], v[4:5], v[40:41]
	v_sub_f32_e32 v20, 0xbfd083aa, v20
	v_med3_f32 v22, v26, s94, v202
	v_add_f32_e32 v11, 1.0, v11
	v_mul_f32_e32 v31, v20, v21
	v_pk_mul_f32 v[20:21], v[22:23], v[188:189]
	v_rcp_f32_e32 v189, v11
	v_sub_f32_e32 v11, 0xbfd083aa, v20
	v_med3_f32 v24, v27, s94, v202
	v_mul_f32_e32 v11, v11, v21
	v_pk_mul_f32 v[20:21], v[24:25], v[188:189]
	v_pk_mul_f32 v[14:15], v[74:75], s[16:17] op_sel_hi:[1,0]
	v_sub_f32_e32 v20, 0xbfd083aa, v20
	v_mul_f32_e32 v32, v20, v21
	v_pk_fma_f32 v[20:21], v[170:171], v[6:7], v[14:15]
	v_pk_fma_f32 v[28:29], v[174:175], v[2:3], v[34:35]
	v_max_f32_e32 v23, 0xc1898193, v20
	v_exp_f32_e32 v20, v23
	v_max_f32_e32 v21, 0xc1898193, v21
	v_med3_f32 v22, v28, s94, v202
	v_pk_mul_f32 v[12:13], v[76:77], s[16:17] op_sel_hi:[1,0]
	v_add_f32_e32 v20, 1.0, v20
	v_rcp_f32_e32 v189, v20
	v_exp_f32_e32 v20, v21
	v_pk_fma_f32 v[24:25], v[172:173], v[8:9], v[12:13]
	v_pk_fma_f32 v[26:27], v[176:177], v[4:5], v[36:37]
	v_pk_mul_f32 v[22:23], v[22:23], v[188:189]
	v_add_f32_e32 v20, 1.0, v20
	v_sub_f32_e32 v22, 0xbfd083aa, v22
	v_mul_f32_e32 v28, v22, v23
	v_max_f32_e32 v23, 0xc1898193, v24
	v_exp_f32_e32 v22, v23
	v_rcp_f32_e32 v189, v20
	v_med3_f32 v20, v29, s94, v202
	v_max_f32_e32 v25, 0xc1898193, v25
	v_add_f32_e32 v22, 1.0, v22
	v_pk_mul_f32 v[20:21], v[20:21], v[188:189]
	v_rcp_f32_e32 v189, v22
	v_exp_f32_e32 v24, v25
	v_sub_f32_e32 v20, 0xbfd083aa, v20
	v_med3_f32 v22, v26, s94, v202
	v_mul_f32_e32 v29, v20, v21
	v_pk_mul_f32 v[20:21], v[22:23], v[188:189]
	v_add_f32_e32 v22, 1.0, v24
	v_rcp_f32_e32 v189, v22
	v_sub_f32_e32 v20, 0xbfd083aa, v20
	v_mul_f32_e32 v26, v20, v21
	v_mov_b32_e32 v21, v187
	v_med3_f32 v24, v27, s94, v202
	v_cvt_pk_fp8_f32 v21, v28, v29
	v_pk_mul_f32 v[22:23], v[24:25], v[188:189]
	v_mov_b32_e32 v20, v187
	v_cvt_pk_fp8_f32 v20, v30, v31
	v_sub_f32_e32 v22, 0xbfd083aa, v22
	v_mul_f32_e32 v22, v22, v23
	v_cvt_pk_fp8_f32 v21, v26, v22 op_sel:[0,0,1]
	v_pk_fma_f32 v[22:23], v[162:163], v[6:7], v[18:19]
	v_cvt_pk_fp8_f32 v20, v11, v32 op_sel:[0,0,1]
	v_max_f32_e32 v25, 0xc1898193, v22
	v_exp_f32_e32 v11, v25
	v_max_f32_e32 v23, 0xc1898193, v23
	v_pk_fma_f32 v[30:31], v[166:167], v[2:3], v[38:39]
	v_pk_fma_f32 v[26:27], v[164:165], v[8:9], v[16:17]
	v_add_f32_e32 v11, 1.0, v11
	v_rcp_f32_e32 v189, v11
	v_exp_f32_e32 v11, v23
	v_med3_f32 v24, v30, s94, v202
	v_max_f32_e32 v27, 0xc1898193, v27
	v_pk_mul_f32 v[24:25], v[24:25], v[188:189]
	v_add_f32_e32 v11, 1.0, v11
	v_sub_f32_e32 v22, 0xbfd083aa, v24
	v_mul_f32_e32 v32, v22, v25
	v_max_f32_e32 v25, 0xc1898193, v26
	v_rcp_f32_e32 v189, v11
	v_exp_f32_e32 v11, v25
	v_med3_f32 v22, v31, s94, v202
	v_pk_fma_f32 v[28:29], v[168:169], v[4:5], v[40:41]
	v_pk_mul_f32 v[22:23], v[22:23], v[188:189]
	v_add_f32_e32 v11, 1.0, v11
	v_rcp_f32_e32 v189, v11
	v_exp_f32_e32 v11, v27
	v_sub_f32_e32 v22, 0xbfd083aa, v22
	v_med3_f32 v24, v28, s94, v202
	v_mul_f32_e32 v33, v22, v23
	v_add_f32_e32 v11, 1.0, v11
	v_pk_mul_f32 v[22:23], v[24:25], v[188:189]
	v_rcp_f32_e32 v189, v11
	v_sub_f32_e32 v11, 0xbfd083aa, v22
	v_med3_f32 v26, v29, s94, v202
	v_mul_f32_e32 v11, v11, v23
	v_pk_mul_f32 v[22:23], v[26:27], v[188:189]
	v_pk_fma_f32 v[30:31], v[158:159], v[2:3], v[34:35]
	v_sub_f32_e32 v22, 0xbfd083aa, v22
	v_mul_f32_e32 v43, v22, v23
	v_pk_fma_f32 v[22:23], v[154:155], v[6:7], v[14:15]
	v_med3_f32 v24, v30, s94, v202
	v_max_f32_e32 v25, 0xc1898193, v22
	v_exp_f32_e32 v22, v25
	v_max_f32_e32 v23, 0xc1898193, v23
	v_pk_fma_f32 v[26:27], v[156:157], v[8:9], v[12:13]
	v_pk_fma_f32 v[28:29], v[160:161], v[4:5], v[36:37]
	v_add_f32_e32 v22, 1.0, v22
	v_rcp_f32_e32 v189, v22
	v_exp_f32_e32 v22, v23
	v_max_f32_e32 v27, 0xc1898193, v27
	s_lshr_b32 s19, s19, 1
	v_pk_mul_f32 v[24:25], v[24:25], v[188:189]
	v_add_f32_e32 v22, 1.0, v22
	v_sub_f32_e32 v24, 0xbfd083aa, v24
	v_mul_f32_e32 v30, v24, v25
	v_max_f32_e32 v25, 0xc1898193, v26
	v_exp_f32_e32 v24, v25
	v_rcp_f32_e32 v189, v22
	v_med3_f32 v22, v31, s94, v202
	v_exp_f32_e32 v26, v27
	v_add_f32_e32 v24, 1.0, v24
	v_pk_mul_f32 v[22:23], v[22:23], v[188:189]
	v_rcp_f32_e32 v189, v24
	v_sub_f32_e32 v22, 0xbfd083aa, v22
	v_med3_f32 v24, v28, s94, v202
	v_mul_f32_e32 v31, v22, v23
	v_pk_mul_f32 v[22:23], v[24:25], v[188:189]
	v_add_f32_e32 v24, 1.0, v26
	v_rcp_f32_e32 v189, v24
	v_sub_f32_e32 v22, 0xbfd083aa, v22
	v_mul_f32_e32 v28, v22, v23
	v_mov_b32_e32 v22, v187
	v_cvt_pk_fp8_f32 v22, v32, v33
	v_mov_b32_e32 v23, v187
	v_med3_f32 v26, v29, s94, v202
	v_cvt_pk_fp8_f32 v23, v30, v31
	v_pk_mul_f32 v[24:25], v[26:27], v[188:189]
	v_cvt_pk_fp8_f32 v22, v11, v43 op_sel:[0,0,1]
	v_sub_f32_e32 v24, 0xbfd083aa, v24
	v_mul_f32_e32 v11, v24, v25
	s_lshl_b32 s21, s26, 7
	s_and_b32 s19, s19, 0x60
	v_cvt_pk_fp8_f32 v23, v28, v11 op_sel:[0,0,1]
	v_ashrrev_i32_e32 v11, 31, v10
	s_or_b32 s26, s19, s21
	v_lshlrev_b64 v[24:25], 11, v[10:11]
	s_ashr_i32 s27, s26, 31
	v_lshl_add_u64 v[24:25], s[12:13], 0, v[24:25]
	v_lshl_add_u64 v[24:25], v[24:25], 0, s[26:27]
	v_permlane16_swap_b32_e32 v20, v22
	v_permlane16_swap_b32_e32 v21, v23
	v_lshl_add_u64 v[24:25], v[24:25], 0, v[186:187]
	global_store_dwordx4 v[24:25], v[20:23], off
	s_cmp_lg_u64 s[14:15], 0
	s_cbranch_scc0 .Lalign7
	s_barrier
; __device__ __forceinline__ unsigned pk4_fp8(float a, float b, float c, float d) { int v = 0; v = __builtin_amdgcn_cvt_pk_fp8_f32(a, b, v, false); v = __builtin_amdgcn_cvt_pk_fp8_f32(c, d, v, true); return (unsigned)v; }
;     __device__ __forceinline__ void operator()(const f32x4 (&acc)[2][2][4][2], const pg8::Unit& u, const Pre& q, int wr, int wc, int fr, int fq) const {
;     ...
;         for (int ai = 0; ai < 2; ++ai)
; #pragma unroll
;             for (int mp = 0; mp < 2; ++mp) { unsigned lo[2], hi[2];
; #pragma unroll
;                 for (int mm = 0; mm < 2; ++mm) { const int m = 2 * mp + mm; float h[8];
; #pragma unroll
;                     for (int n = 0; n < 2; ++n) { const f32x4 gk = __builtin_elementwise_fma(acc[ai][0][m][n], dsk, q.bg[n]), up = __builtin_elementwise_fma(acc[ai][1][m][n], dsu, q.bu[n]);
; #pragma unroll
;                         for (int j = 0; j < 4; ++j) { const float gm = __builtin_fmaxf(gk[j], 7.0f * KP), li = __builtin_amdgcn_fmed3f(up[j], -7.0f, 7.0f);
;                             const float sg = __builtin_amdgcn_rcpf(1.0f + __builtin_amdgcn_exp2f(gm));
;                             h[n * 4 + j] = (gm * sg) * (li * (FP8_SH / KP) + (FP8_SH / KP)); } }
;                     lo[mm] = pk4_fp8(h[0], h[1], h[2], h[3]); hi[mm] = pk4_fp8(h[4], h[5], h[6], h[7]); }
;                 const v2u r0 = __builtin_amdgcn_permlane16_swap(lo[0], lo[1], false, false), r1 = __builtin_amdgcn_permlane16_swap(hi[0], hi[1], false, false);
;                 unsigned char* rowp = hb + (size_t)(row0 + ai * 128 + (2 * mp + (fq & 1)) * 16) * FF + f0w + 16 * (fq >> 1);
;                 *(v4u*)rowp = (v4u){r0.x, r1.x, r0.y, r1.y}; }
.Lalign7:
	v_pk_fma_f32 v[28:29], v[150:151], v[2:3], v[38:39]
	v_pk_fma_f32 v[24:25], v[148:149], v[8:9], v[16:17]
	v_pk_fma_f32 v[20:21], v[146:147], v[6:7], v[18:19]
	v_med3_f32 v22, v28, s94, v202
	v_max_f32_e32 v23, 0xc1898193, v20
	v_exp_f32_e32 v11, v23
	v_max_f32_e32 v21, 0xc1898193, v21
	v_max_f32_e32 v25, 0xc1898193, v25
	v_pk_fma_f32 v[26:27], v[152:153], v[4:5], v[40:41]
	v_add_f32_e32 v11, 1.0, v11
	v_rcp_f32_e32 v189, v11
	v_exp_f32_e32 v11, v21
	s_andn2_b64 vcc, exec, s[2:3]
	s_mov_b64 s[2:3], -1
	v_pk_mul_f32 v[22:23], v[22:23], v[188:189]
	v_add_f32_e32 v11, 1.0, v11
	v_sub_f32_e32 v20, 0xbfd083aa, v22
	v_mul_f32_e32 v30, v20, v23
	v_max_f32_e32 v23, 0xc1898193, v24
	v_rcp_f32_e32 v189, v11
	v_exp_f32_e32 v11, v23
	v_med3_f32 v20, v29, s94, v202
	v_med3_f32 v22, v26, s94, v202
	v_pk_mul_f32 v[20:21], v[20:21], v[188:189]
	v_add_f32_e32 v11, 1.0, v11
	v_rcp_f32_e32 v189, v11
	v_exp_f32_e32 v11, v25
	v_sub_f32_e32 v20, 0xbfd083aa, v20
	v_mul_f32_e32 v31, v20, v21
	v_pk_mul_f32 v[20:21], v[22:23], v[188:189]
	v_add_f32_e32 v11, 1.0, v11
	v_rcp_f32_e32 v189, v11
	v_sub_f32_e32 v11, 0xbfd083aa, v20
	v_med3_f32 v24, v27, s94, v202
	v_mul_f32_e32 v11, v11, v21
	v_pk_mul_f32 v[20:21], v[24:25], v[188:189]
	v_pk_fma_f32 v[28:29], v[142:143], v[2:3], v[34:35]
	v_sub_f32_e32 v20, 0xbfd083aa, v20
	v_mul_f32_e32 v32, v20, v21
	v_pk_fma_f32 v[20:21], v[138:139], v[6:7], v[14:15]
	v_med3_f32 v22, v28, s94, v202
	v_max_f32_e32 v23, 0xc1898193, v20
	v_exp_f32_e32 v20, v23
	v_max_f32_e32 v21, 0xc1898193, v21
	v_pk_fma_f32 v[24:25], v[140:141], v[8:9], v[12:13]
	v_pk_fma_f32 v[26:27], v[144:145], v[4:5], v[36:37]
	v_add_f32_e32 v20, 1.0, v20
	v_rcp_f32_e32 v189, v20
	v_exp_f32_e32 v20, v21
	v_max_f32_e32 v25, 0xc1898193, v25
	v_pk_mul_f32 v[22:23], v[22:23], v[188:189]
	s_nop 0
	v_sub_f32_e32 v22, 0xbfd083aa, v22
	v_mul_f32_e32 v28, v22, v23
	v_max_f32_e32 v23, 0xc1898193, v24
	v_add_f32_e32 v20, 1.0, v20
	v_exp_f32_e32 v22, v23
	v_rcp_f32_e32 v189, v20
	v_med3_f32 v20, v29, s94, v202
	v_exp_f32_e32 v24, v25
	v_add_f32_e32 v22, 1.0, v22
	v_pk_mul_f32 v[20:21], v[20:21], v[188:189]
	v_rcp_f32_e32 v189, v22
	v_sub_f32_e32 v20, 0xbfd083aa, v20
	v_med3_f32 v22, v26, s94, v202
	v_mul_f32_e32 v29, v20, v21
	v_pk_mul_f32 v[20:21], v[22:23], v[188:189]
	v_add_f32_e32 v22, 1.0, v24
	v_rcp_f32_e32 v189, v22
	v_sub_f32_e32 v20, 0xbfd083aa, v20
	v_mul_f32_e32 v26, v20, v21
	v_mov_b32_e32 v21, v187
	v_med3_f32 v24, v27, s94, v202
	v_cvt_pk_fp8_f32 v21, v28, v29
	v_pk_mul_f32 v[22:23], v[24:25], v[188:189]
	v_mov_b32_e32 v20, v187
	v_cvt_pk_fp8_f32 v20, v30, v31
	v_sub_f32_e32 v22, 0xbfd083aa, v22
	v_mul_f32_e32 v22, v22, v23
	v_cvt_pk_fp8_f32 v21, v26, v22 op_sel:[0,0,1]
	v_pk_fma_f32 v[22:23], v[130:131], v[6:7], v[18:19]
	v_cvt_pk_fp8_f32 v20, v11, v32 op_sel:[0,0,1]
	v_max_f32_e32 v25, 0xc1898193, v22
	v_exp_f32_e32 v11, v25
	v_max_f32_e32 v23, 0xc1898193, v23
	v_pk_fma_f32 v[30:31], v[134:135], v[2:3], v[38:39]
	v_pk_fma_f32 v[26:27], v[132:133], v[8:9], v[16:17]
	v_add_f32_e32 v11, 1.0, v11
	v_rcp_f32_e32 v189, v11
	v_exp_f32_e32 v11, v23
	v_med3_f32 v24, v30, s94, v202
	v_max_f32_e32 v27, 0xc1898193, v27
	v_pk_mul_f32 v[24:25], v[24:25], v[188:189]
	v_add_f32_e32 v11, 1.0, v11
	v_sub_f32_e32 v22, 0xbfd083aa, v24
	v_mul_f32_e32 v32, v22, v25
	v_max_f32_e32 v25, 0xc1898193, v26
	v_rcp_f32_e32 v189, v11
	v_exp_f32_e32 v11, v25
	v_med3_f32 v22, v31, s94, v202
	v_pk_fma_f32 v[28:29], v[136:137], v[4:5], v[40:41]
	v_pk_mul_f32 v[22:23], v[22:23], v[188:189]
	v_add_f32_e32 v11, 1.0, v11
	v_rcp_f32_e32 v189, v11
	v_exp_f32_e32 v11, v27
	v_sub_f32_e32 v22, 0xbfd083aa, v22
	v_med3_f32 v24, v28, s94, v202
	v_mul_f32_e32 v33, v22, v23
	v_add_f32_e32 v11, 1.0, v11
	v_pk_mul_f32 v[22:23], v[24:25], v[188:189]
	v_rcp_f32_e32 v189, v11
	v_sub_f32_e32 v11, 0xbfd083aa, v22
	v_med3_f32 v26, v29, s94, v202
	v_mul_f32_e32 v11, v11, v23
	v_pk_mul_f32 v[22:23], v[26:27], v[188:189]
	v_pk_fma_f32 v[30:31], v[126:127], v[2:3], v[34:35]
	v_sub_f32_e32 v22, 0xbfd083aa, v22
	v_mul_f32_e32 v43, v22, v23
	v_pk_fma_f32 v[22:23], v[122:123], v[6:7], v[14:15]
	v_med3_f32 v24, v30, s94, v202
	v_max_f32_e32 v25, 0xc1898193, v22
	v_exp_f32_e32 v22, v25
	v_max_f32_e32 v23, 0xc1898193, v23
	v_pk_fma_f32 v[26:27], v[124:125], v[8:9], v[12:13]
	v_pk_fma_f32 v[28:29], v[128:129], v[4:5], v[36:37]
	v_add_f32_e32 v22, 1.0, v22
	v_rcp_f32_e32 v189, v22
	v_exp_f32_e32 v22, v23
	v_max_f32_e32 v27, 0xc1898193, v27
	v_pk_mul_f32 v[24:25], v[24:25], v[188:189]
	s_nop 0
	v_sub_f32_e32 v24, 0xbfd083aa, v24
	v_mul_f32_e32 v30, v24, v25
	v_max_f32_e32 v25, 0xc1898193, v26
	v_add_f32_e32 v22, 1.0, v22
	v_exp_f32_e32 v24, v25
	v_rcp_f32_e32 v189, v22
	v_med3_f32 v22, v31, s94, v202
	v_exp_f32_e32 v26, v27
	v_add_f32_e32 v24, 1.0, v24
	v_pk_mul_f32 v[22:23], v[22:23], v[188:189]
	v_rcp_f32_e32 v189, v24
	v_sub_f32_e32 v22, 0xbfd083aa, v22
	v_med3_f32 v24, v28, s94, v202
	v_mul_f32_e32 v31, v22, v23
	v_pk_mul_f32 v[22:23], v[24:25], v[188:189]
	v_add_f32_e32 v24, 1.0, v26
	v_rcp_f32_e32 v189, v24
	v_sub_f32_e32 v22, 0xbfd083aa, v22
	v_mul_f32_e32 v28, v22, v23
	v_mov_b32_e32 v22, v187
	v_cvt_pk_fp8_f32 v22, v32, v33
	v_mov_b32_e32 v23, v187
	v_med3_f32 v26, v29, s94, v202
	v_cvt_pk_fp8_f32 v23, v30, v31
	v_pk_mul_f32 v[24:25], v[26:27], v[188:189]
	v_cvt_pk_fp8_f32 v22, v11, v43 op_sel:[0,0,1]
	v_sub_f32_e32 v24, 0xbfd083aa, v24
	v_mul_f32_e32 v11, v24, v25
	v_or_b32_e32 v24, 32, v10
	v_cvt_pk_fp8_f32 v23, v28, v11 op_sel:[0,0,1]
	v_ashrrev_i32_e32 v25, 31, v24
	v_lshlrev_b64 v[24:25], 11, v[24:25]
	v_lshl_add_u64 v[24:25], s[12:13], 0, v[24:25]
	v_lshl_add_u64 v[24:25], v[24:25], 0, s[26:27]
; __device__ __forceinline__ unsigned pk4_fp8(float a, float b, float c, float d) { int v = 0; v = __builtin_amdgcn_cvt_pk_fp8_f32(a, b, v, false); v = __builtin_amdgcn_cvt_pk_fp8_f32(c, d, v, true); return (unsigned)v; }
;     __device__ __forceinline__ void operator()(const f32x4 (&acc)[2][2][4][2], const pg8::Unit& u, const Pre& q, int wr, int wc, int fr, int fq) const {
;     ...
;         for (int ai = 0; ai < 2; ++ai)
; #pragma unroll
;             for (int mp = 0; mp < 2; ++mp) { unsigned lo[2], hi[2];
; #pragma unroll
;                 for (int mm = 0; mm < 2; ++mm) { const int m = 2 * mp + mm; float h[8];
; #pragma unroll
;                     for (int n = 0; n < 2; ++n) { const f32x4 gk = __builtin_elementwise_fma(acc[ai][0][m][n], dsk, q.bg[n]), up = __builtin_elementwise_fma(acc[ai][1][m][n], dsu, q.bu[n]);
; #pragma unroll
;                         for (int j = 0; j < 4; ++j) { const float gm = __builtin_fmaxf(gk[j], 7.0f * KP), li = __builtin_amdgcn_fmed3f(up[j], -7.0f, 7.0f);
;                             const float sg = __builtin_amdgcn_rcpf(1.0f + __builtin_amdgcn_exp2f(gm));
;                             h[n * 4 + j] = (gm * sg) * (li * (FP8_SH / KP) + (FP8_SH / KP)); } }
;                     lo[mm] = pk4_fp8(h[0], h[1], h[2], h[3]); hi[mm] = pk4_fp8(h[4], h[5], h[6], h[7]); }
;                 const v2u r0 = __builtin_amdgcn_permlane16_swap(lo[0], lo[1], false, false), r1 = __builtin_amdgcn_permlane16_swap(hi[0], hi[1], false, false);
;                 unsigned char* rowp = hb + (size_t)(row0 + ai * 128 + (2 * mp + (fq & 1)) * 16) * FF + f0w + 16 * (fq >> 1);
;                 *(v4u*)rowp = (v4u){r0.x, r1.x, r0.y, r1.y}; }
	v_permlane16_swap_b32_e32 v20, v22
	v_permlane16_swap_b32_e32 v21, v23
	v_lshl_add_u64 v[24:25], v[24:25], 0, v[186:187]
	global_store_dwordx4 v[24:25], v[20:23], off
	v_pk_fma_f32 v[30:31], v[106:107], v[2:3], v[38:39]
	v_pk_fma_f32 v[26:27], v[120:121], v[8:9], v[16:17]
	v_pk_fma_f32 v[22:23], v[118:119], v[6:7], v[18:19]
	v_med3_f32 v24, v30, s94, v202
	v_max_f32_e32 v25, 0xc1898193, v22
	v_exp_f32_e32 v11, v25
	v_max_f32_e32 v23, 0xc1898193, v23
	v_med3_f32 v22, v31, s94, v202
	v_max_f32_e32 v27, 0xc1898193, v27
	v_add_f32_e32 v11, 1.0, v11
	v_rcp_f32_e32 v189, v11
	v_exp_f32_e32 v11, v23
	v_pk_fma_f32 v[28:29], v[108:109], v[4:5], v[40:41]
	v_pk_fma_f32 v[30:31], v[114:115], v[2:3], v[34:35]
	v_pk_mul_f32 v[24:25], v[24:25], v[188:189]
	v_add_f32_e32 v11, 1.0, v11
	v_sub_f32_e32 v21, 0xbfd083aa, v24
	v_mul_f32_e32 v21, v21, v25
	v_max_f32_e32 v25, 0xc1898193, v26
	v_rcp_f32_e32 v189, v11
	v_exp_f32_e32 v11, v25
	v_med3_f32 v24, v28, s94, v202
	v_med3_f32 v26, v29, s94, v202
	v_pk_mul_f32 v[22:23], v[22:23], v[188:189]
	v_add_f32_e32 v11, 1.0, v11
	v_rcp_f32_e32 v189, v11
	v_exp_f32_e32 v11, v27
	v_sub_f32_e32 v22, 0xbfd083aa, v22
	v_mul_f32_e32 v32, v22, v23
	v_pk_mul_f32 v[22:23], v[24:25], v[188:189]
	v_add_f32_e32 v11, 1.0, v11
	v_rcp_f32_e32 v189, v11
	v_sub_f32_e32 v11, 0xbfd083aa, v22
	v_mul_f32_e32 v11, v11, v23
	v_med3_f32 v24, v30, s94, v202
	v_pk_mul_f32 v[22:23], v[26:27], v[188:189]
	v_pk_fma_f32 v[26:27], v[112:113], v[8:9], v[12:13]
	v_sub_f32_e32 v22, 0xbfd083aa, v22
	v_mul_f32_e32 v33, v22, v23
	v_pk_fma_f32 v[22:23], v[110:111], v[6:7], v[14:15]
	v_max_f32_e32 v27, 0xc1898193, v27
	v_max_f32_e32 v25, 0xc1898193, v22
	v_exp_f32_e32 v22, v25
	v_max_f32_e32 v23, 0xc1898193, v23
	v_pk_fma_f32 v[28:29], v[116:117], v[4:5], v[36:37]
	v_add_u32_e32 v20, 0x80, v10
	v_add_f32_e32 v22, 1.0, v22
	v_rcp_f32_e32 v189, v22
	v_exp_f32_e32 v22, v23
	v_pk_mul_f32 v[24:25], v[24:25], v[188:189]
	s_nop 0
	v_sub_f32_e32 v24, 0xbfd083aa, v24
	v_mul_f32_e32 v30, v24, v25
	v_max_f32_e32 v25, 0xc1898193, v26
	v_add_f32_e32 v22, 1.0, v22
	v_exp_f32_e32 v24, v25
	v_rcp_f32_e32 v189, v22
	v_med3_f32 v22, v31, s94, v202
	v_exp_f32_e32 v26, v27
	v_add_f32_e32 v24, 1.0, v24
	v_pk_mul_f32 v[22:23], v[22:23], v[188:189]
	v_rcp_f32_e32 v189, v24
	v_sub_f32_e32 v22, 0xbfd083aa, v22
	v_med3_f32 v24, v28, s94, v202
	v_mul_f32_e32 v31, v22, v23
	v_pk_mul_f32 v[22:23], v[24:25], v[188:189]
	v_add_f32_e32 v24, 1.0, v26
	v_rcp_f32_e32 v189, v24
	v_sub_f32_e32 v22, 0xbfd083aa, v22
	v_mul_f32_e32 v28, v22, v23
	v_med3_f32 v26, v29, s94, v202
	v_mov_b32_e32 v22, v187
	v_pk_mul_f32 v[24:25], v[26:27], v[188:189]
	v_cvt_pk_fp8_f32 v22, v21, v32
	v_sub_f32_e32 v21, 0xbfd083aa, v24
	v_mul_f32_e32 v21, v21, v25
	v_pk_fma_f32 v[24:25], v[98:99], v[6:7], v[18:19]
	v_cvt_pk_fp8_f32 v22, v11, v33 op_sel:[0,0,1]
	v_max_f32_e32 v27, 0xc1898193, v24
	v_exp_f32_e32 v11, v27
	v_mov_b32_e32 v23, v187
	v_cvt_pk_fp8_f32 v23, v30, v31
	v_max_f32_e32 v25, 0xc1898193, v25
	v_add_f32_e32 v11, 1.0, v11
	v_rcp_f32_e32 v189, v11
	v_pk_fma_f32 v[32:33], v[102:103], v[2:3], v[38:39]
	v_exp_f32_e32 v11, v25
	v_med3_f32 v26, v32, s94, v202
	v_pk_mul_f32 v[26:27], v[26:27], v[188:189]
	v_cvt_pk_fp8_f32 v23, v28, v21 op_sel:[0,0,1]
	v_pk_fma_f32 v[28:29], v[100:101], v[8:9], v[16:17]
	v_sub_f32_e32 v21, 0xbfd083aa, v26
	v_mul_f32_e32 v21, v21, v27
	v_add_f32_e32 v11, 1.0, v11
	v_max_f32_e32 v27, 0xc1898193, v28
	v_rcp_f32_e32 v189, v11
	v_exp_f32_e32 v11, v27
	v_med3_f32 v24, v33, s94, v202
	v_max_f32_e32 v29, 0xc1898193, v29
	v_pk_mul_f32 v[24:25], v[24:25], v[188:189]
	v_add_f32_e32 v11, 1.0, v11
	v_rcp_f32_e32 v189, v11
	v_exp_f32_e32 v11, v29
	v_pk_fma_f32 v[30:31], v[104:105], v[4:5], v[40:41]
	v_sub_f32_e32 v24, 0xbfd083aa, v24
	v_med3_f32 v26, v30, s94, v202
	v_add_f32_e32 v11, 1.0, v11
	v_mul_f32_e32 v43, v24, v25
	v_pk_mul_f32 v[24:25], v[26:27], v[188:189]
	v_rcp_f32_e32 v189, v11
	v_sub_f32_e32 v11, 0xbfd083aa, v24
	v_med3_f32 v28, v31, s94, v202
	v_mul_f32_e32 v11, v11, v25
	v_pk_mul_f32 v[24:25], v[28:29], v[188:189]
	v_pk_fma_f32 v[32:33], v[94:95], v[2:3], v[34:35]
	v_sub_f32_e32 v24, 0xbfd083aa, v24
	v_mul_f32_e32 v44, v24, v25
	v_pk_fma_f32 v[24:25], v[90:91], v[6:7], v[14:15]
	v_med3_f32 v26, v32, s94, v202
	v_max_f32_e32 v27, 0xc1898193, v24
	v_exp_f32_e32 v24, v27
	v_max_f32_e32 v25, 0xc1898193, v25
	v_pk_fma_f32 v[28:29], v[92:93], v[8:9], v[12:13]
	v_pk_fma_f32 v[30:31], v[96:97], v[4:5], v[36:37]
	v_add_f32_e32 v24, 1.0, v24
	v_rcp_f32_e32 v189, v24
	v_exp_f32_e32 v24, v25
	v_max_f32_e32 v29, 0xc1898193, v29
	v_pk_mul_f32 v[26:27], v[26:27], v[188:189]
	s_nop 0
	v_sub_f32_e32 v26, 0xbfd083aa, v26
	v_mul_f32_e32 v32, v26, v27
	v_max_f32_e32 v27, 0xc1898193, v28
	v_add_f32_e32 v24, 1.0, v24
	v_exp_f32_e32 v26, v27
	v_rcp_f32_e32 v189, v24
	v_med3_f32 v24, v33, s94, v202
	v_exp_f32_e32 v28, v29
	v_add_f32_e32 v26, 1.0, v26
	v_pk_mul_f32 v[24:25], v[24:25], v[188:189]
	v_rcp_f32_e32 v189, v26
	v_sub_f32_e32 v24, 0xbfd083aa, v24
	v_med3_f32 v26, v30, s94, v202
	v_mul_f32_e32 v33, v24, v25
	v_pk_mul_f32 v[24:25], v[26:27], v[188:189]
	v_add_f32_e32 v26, 1.0, v28
	v_rcp_f32_e32 v189, v26
	v_sub_f32_e32 v24, 0xbfd083aa, v24
	v_mul_f32_e32 v30, v24, v25
	v_mov_b32_e32 v24, v187
	v_cvt_pk_fp8_f32 v24, v21, v43
	v_mov_b32_e32 v25, v187
	v_med3_f32 v28, v31, s94, v202
	v_cvt_pk_fp8_f32 v25, v32, v33
	v_pk_mul_f32 v[26:27], v[28:29], v[188:189]
	v_cvt_pk_fp8_f32 v24, v11, v44 op_sel:[0,0,1]
	v_sub_f32_e32 v21, 0xbfd083aa, v26
	v_mul_f32_e32 v11, v21, v27
	v_cvt_pk_fp8_f32 v25, v30, v11 op_sel:[0,0,1]
	v_ashrrev_i32_e32 v21, 31, v20
	v_lshlrev_b64 v[20:21], 11, v[20:21]
; __device__ __forceinline__ unsigned pk4_fp8(float a, float b, float c, float d) { int v = 0; v = __builtin_amdgcn_cvt_pk_fp8_f32(a, b, v, false); v = __builtin_amdgcn_cvt_pk_fp8_f32(c, d, v, true); return (unsigned)v; }
;     __device__ __forceinline__ void operator()(const f32x4 (&acc)[2][2][4][2], const pg8::Unit& u, const Pre& q, int wr, int wc, int fr, int fq) const {
;     ...
;         for (int ai = 0; ai < 2; ++ai)
; #pragma unroll
;             for (int mp = 0; mp < 2; ++mp) { unsigned lo[2], hi[2];
; #pragma unroll
;                 for (int mm = 0; mm < 2; ++mm) { const int m = 2 * mp + mm; float h[8];
; #pragma unroll
;                     for (int n = 0; n < 2; ++n) { const f32x4 gk = __builtin_elementwise_fma(acc[ai][0][m][n], dsk, q.bg[n]), up = __builtin_elementwise_fma(acc[ai][1][m][n], dsu, q.bu[n]);
; #pragma unroll
;                         for (int j = 0; j < 4; ++j) { const float gm = __builtin_fmaxf(gk[j], 7.0f * KP), li = __builtin_amdgcn_fmed3f(up[j], -7.0f, 7.0f);
;                             const float sg = __builtin_amdgcn_rcpf(1.0f + __builtin_amdgcn_exp2f(gm));
;                             h[n * 4 + j] = (gm * sg) * (li * (FP8_SH / KP) + (FP8_SH / KP)); } }
;                     lo[mm] = pk4_fp8(h[0], h[1], h[2], h[3]); hi[mm] = pk4_fp8(h[4], h[5], h[6], h[7]); }
;                 const v2u r0 = __builtin_amdgcn_permlane16_swap(lo[0], lo[1], false, false), r1 = __builtin_amdgcn_permlane16_swap(hi[0], hi[1], false, false);
;                 unsigned char* rowp = hb + (size_t)(row0 + ai * 128 + (2 * mp + (fq & 1)) * 16) * FF + f0w + 16 * (fq >> 1);
;                 *(v4u*)rowp = (v4u){r0.x, r1.x, r0.y, r1.y}; }
	v_lshl_add_u64 v[20:21], s[12:13], 0, v[20:21]
	v_lshl_add_u64 v[20:21], v[20:21], 0, s[26:27]
	v_permlane16_swap_b32_e32 v22, v24
	v_permlane16_swap_b32_e32 v23, v25
	v_lshl_add_u64 v[20:21], v[20:21], 0, v[186:187]
	global_store_dwordx4 v[20:21], v[22:25], off
	v_pk_fma_f32 v[20:21], v[82:83], v[6:7], v[18:19]
	v_pk_fma_f32 v[28:29], v[86:87], v[2:3], v[38:39]
	v_max_f32_e32 v23, 0xc1898193, v20
	v_exp_f32_e32 v11, v23
	v_max_f32_e32 v21, 0xc1898193, v21
	v_med3_f32 v22, v28, s94, v202
	v_pk_fma_f32 v[24:25], v[84:85], v[8:9], v[16:17]
	v_add_f32_e32 v11, 1.0, v11
	v_rcp_f32_e32 v189, v11
	v_exp_f32_e32 v11, v21
	v_max_f32_e32 v25, 0xc1898193, v25
	v_pk_fma_f32 v[26:27], v[88:89], v[4:5], v[40:41]
	v_pk_mul_f32 v[22:23], v[22:23], v[188:189]
	v_add_f32_e32 v11, 1.0, v11
	v_sub_f32_e32 v20, 0xbfd083aa, v22
	v_mul_f32_e32 v30, v20, v23
	v_max_f32_e32 v23, 0xc1898193, v24
	v_rcp_f32_e32 v189, v11
	v_exp_f32_e32 v11, v23
	v_med3_f32 v20, v29, s94, v202
	v_med3_f32 v22, v26, s94, v202
	v_pk_mul_f32 v[20:21], v[20:21], v[188:189]
	v_add_f32_e32 v11, 1.0, v11
	v_rcp_f32_e32 v189, v11
	v_exp_f32_e32 v11, v25
	v_sub_f32_e32 v20, 0xbfd083aa, v20
	v_mul_f32_e32 v31, v20, v21
	v_pk_mul_f32 v[20:21], v[22:23], v[188:189]
	v_add_f32_e32 v11, 1.0, v11
	v_rcp_f32_e32 v189, v11
	v_sub_f32_e32 v11, 0xbfd083aa, v20
	v_med3_f32 v24, v27, s94, v202
	v_mul_f32_e32 v11, v11, v21
	v_pk_mul_f32 v[20:21], v[24:25], v[188:189]
	v_pk_fma_f32 v[28:29], v[70:71], v[2:3], v[34:35]
	v_sub_f32_e32 v20, 0xbfd083aa, v20
	v_mul_f32_e32 v32, v20, v21
	v_pk_fma_f32 v[20:21], v[66:67], v[6:7], v[14:15]
	v_med3_f32 v22, v28, s94, v202
	v_max_f32_e32 v23, 0xc1898193, v20
	v_exp_f32_e32 v20, v23
	v_max_f32_e32 v21, 0xc1898193, v21
	v_pk_fma_f32 v[24:25], v[68:69], v[8:9], v[12:13]
	v_pk_fma_f32 v[26:27], v[72:73], v[4:5], v[36:37]
	v_add_f32_e32 v20, 1.0, v20
	v_rcp_f32_e32 v189, v20
	v_exp_f32_e32 v20, v21
	v_max_f32_e32 v25, 0xc1898193, v25
	v_pk_fma_f32 v[18:19], v[58:59], v[6:7], v[18:19]
	v_pk_mul_f32 v[22:23], v[22:23], v[188:189]
	v_add_f32_e32 v20, 1.0, v20
	v_sub_f32_e32 v22, 0xbfd083aa, v22
	v_mul_f32_e32 v28, v22, v23
	v_max_f32_e32 v23, 0xc1898193, v24
	v_exp_f32_e32 v22, v23
	v_rcp_f32_e32 v189, v20
	v_med3_f32 v20, v29, s94, v202
	v_exp_f32_e32 v24, v25
	v_add_f32_e32 v22, 1.0, v22
	v_pk_mul_f32 v[20:21], v[20:21], v[188:189]
	v_rcp_f32_e32 v189, v22
	v_sub_f32_e32 v20, 0xbfd083aa, v20
	v_med3_f32 v22, v26, s94, v202
	v_mul_f32_e32 v29, v20, v21
	v_pk_mul_f32 v[20:21], v[22:23], v[188:189]
	v_add_f32_e32 v22, 1.0, v24
	v_rcp_f32_e32 v189, v22
	v_sub_f32_e32 v20, 0xbfd083aa, v20
	v_mul_f32_e32 v26, v20, v21
	v_mov_b32_e32 v20, v187
	v_med3_f32 v24, v27, s94, v202
	v_cvt_pk_fp8_f32 v20, v30, v31
	v_pk_mul_f32 v[22:23], v[24:25], v[188:189]
	v_mov_b32_e32 v21, v187
	v_sub_f32_e32 v22, 0xbfd083aa, v22
	v_mul_f32_e32 v22, v22, v23
	v_max_f32_e32 v23, 0xc1898193, v18
	v_cvt_pk_fp8_f32 v20, v11, v32 op_sel:[0,0,1]
	v_exp_f32_e32 v11, v23
	v_cvt_pk_fp8_f32 v21, v28, v29
	v_max_f32_e32 v19, 0xc1898193, v19
	v_pk_fma_f32 v[16:17], v[60:61], v[8:9], v[16:17]
	v_add_f32_e32 v11, 1.0, v11
	v_rcp_f32_e32 v189, v11
	v_cvt_pk_fp8_f32 v21, v26, v22 op_sel:[0,0,1]
	v_pk_fma_f32 v[26:27], v[62:63], v[2:3], v[38:39]
	v_exp_f32_e32 v11, v19
	v_med3_f32 v22, v26, s94, v202
	v_pk_mul_f32 v[22:23], v[22:23], v[188:189]
	v_max_f32_e32 v17, 0xc1898193, v17
	v_sub_f32_e32 v18, 0xbfd083aa, v22
	v_mul_f32_e32 v26, v18, v23
	v_add_f32_e32 v11, 1.0, v11
	v_max_f32_e32 v23, 0xc1898193, v16
	v_rcp_f32_e32 v189, v11
	v_exp_f32_e32 v11, v23
	v_med3_f32 v18, v27, s94, v202
	v_pk_fma_f32 v[6:7], v[50:51], v[6:7], v[14:15]
	v_pk_mul_f32 v[18:19], v[18:19], v[188:189]
	v_add_f32_e32 v11, 1.0, v11
	v_rcp_f32_e32 v189, v11
	v_exp_f32_e32 v11, v17
	v_pk_fma_f32 v[24:25], v[64:65], v[4:5], v[40:41]
	v_max_f32_e32 v15, 0xc1898193, v6
	v_sub_f32_e32 v16, 0xbfd083aa, v18
	v_med3_f32 v22, v24, s94, v202
	v_add_f32_e32 v11, 1.0, v11
	v_exp_f32_e32 v6, v15
	v_mul_f32_e32 v27, v16, v19
	v_pk_mul_f32 v[18:19], v[22:23], v[188:189]
	v_rcp_f32_e32 v189, v11
	v_med3_f32 v16, v25, s94, v202
	v_add_f32_e32 v6, 1.0, v6
	v_pk_fma_f32 v[2:3], v[54:55], v[2:3], v[34:35]
	v_pk_mul_f32 v[16:17], v[16:17], v[188:189]
	v_rcp_f32_e32 v189, v6
	v_max_f32_e32 v7, 0xc1898193, v7
	v_med3_f32 v14, v2, s94, v202
	v_exp_f32_e32 v2, v7
	v_pk_fma_f32 v[8:9], v[52:53], v[8:9], v[12:13]
	v_pk_mul_f32 v[12:13], v[14:15], v[188:189]
	v_pk_fma_f32 v[4:5], v[56:57], v[4:5], v[36:37]
	v_sub_f32_e32 v6, 0xbfd083aa, v12
	v_mul_f32_e32 v14, v6, v13
	v_add_f32_e32 v2, 1.0, v2
	v_max_f32_e32 v13, 0xc1898193, v8
	v_rcp_f32_e32 v189, v2
	v_exp_f32_e32 v8, v13
	v_med3_f32 v6, v3, s94, v202
	v_med3_f32 v12, v4, s94, v202
	v_pk_mul_f32 v[2:3], v[6:7], v[188:189]
	v_add_f32_e32 v6, 1.0, v8
	v_max_f32_e32 v7, 0xc1898193, v9
	v_rcp_f32_e32 v189, v6
	v_exp_f32_e32 v6, v7
	v_sub_f32_e32 v2, 0xbfd083aa, v2
	v_mul_f32_e32 v8, v2, v3
	v_pk_mul_f32 v[2:3], v[12:13], v[188:189]
	v_add_f32_e32 v4, 1.0, v6
	v_rcp_f32_e32 v189, v4
	v_mov_b32_e32 v23, v187
	v_sub_f32_e32 v2, 0xbfd083aa, v2
	v_med3_f32 v6, v5, s94, v202
	v_mov_b32_e32 v22, v187
	v_cvt_pk_fp8_f32 v23, v14, v8
	v_mul_f32_e32 v4, v2, v3
	v_pk_mul_f32 v[2:3], v[6:7], v[188:189]
	v_cvt_pk_fp8_f32 v22, v26, v27
	v_sub_f32_e32 v2, 0xbfd083aa, v2
	v_sub_f32_e32 v11, 0xbfd083aa, v18
	v_sub_f32_e32 v16, 0xbfd083aa, v16
	v_mul_f32_e32 v2, v2, v3
	v_mul_f32_e32 v11, v11, v19
	v_mul_f32_e32 v16, v16, v17
	v_cvt_pk_fp8_f32 v23, v4, v2 op_sel:[0,0,1]
	v_add_u32_e32 v2, 0xa0, v10
	v_cvt_pk_fp8_f32 v22, v11, v16 op_sel:[0,0,1]
	v_ashrrev_i32_e32 v3, 31, v2
	v_lshlrev_b64 v[2:3], 11, v[2:3]
	v_lshl_add_u64 v[2:3], s[12:13], 0, v[2:3]
	v_lshl_add_u64 v[2:3], v[2:3], 0, s[26:27]
	v_permlane16_swap_b32_e32 v20, v22
	v_permlane16_swap_b32_e32 v21, v23
	v_lshl_add_u64 v[2:3], v[2:3], 0, v[186:187]
	global_store_dwordx4 v[2:3], v[20:23], off
	s_cbranch_vccnz .LBB0_726
; #define PG8_BAR __builtin_amdgcn_s_barrier()
; template <class Epi, class Sched>
; __device__ __forceinline__ void gemm_phase(LAS unsigned char* lds, const Sched& S, const Epi& E) {
;     ...
;         cur = nxt; cA = nA; cB = nB; crot = nrot; ++ui;
;         E.prefetch(cur, epre);
;         if (wr == 1) PG8_BAR;
;     __device__ __forceinline__ void prefetch(const pg8::Unit& u, Pre& q) const {
;         int tz = threadIdx.x; asm volatile("" : "+v"(tz)); const int wc = (tz >> 6) & 3, fq = (tz >> 4) & 3;
;         const int f0 = u.pn * 128 + wc * 32 + 8 * fq;
; #pragma unroll
;         for (int n = 0; n < 2; ++n) { q.bg[n] = *(const f32x4*)(b_gate + (size_t)u.e * FF + f0 + 4 * n) * KP; q.bu[n] = *(const f32x4*)(b_up + (size_t)u.e * FF + f0 + 4 * n); }
;     }
	v_mov_b32_e32 v2, v0
	s_ashr_i32 s21, s20, 31
	v_readlane_b32 s72, v255, 29
	v_lshrrev_b32_e32 v2, 1, v2
	s_lshl_b64 s[2:3], s[20:21], 13
	v_readlane_b32 s76, v255, 33
	v_and_b32_e32 v2, 0x78, v2
	v_readlane_b32 s77, v255, 34
	s_add_u32 s26, s76, s2
	v_lshl_or_b32 v2, s44, 7, v2
	v_readlane_b32 s80, v255, 37
	s_addc_u32 s27, s77, s3
	v_ashrrev_i32_e32 v3, 31, v2
	v_readlane_b32 s81, v255, 38
	s_add_u32 s2, s80, s2
	v_lshlrev_b64 v[2:3], 2, v[2:3]
	s_addc_u32 s3, s81, s3
	v_lshl_add_u64 v[4:5], s[26:27], 0, v[2:3]
	v_lshl_add_u64 v[2:3], s[2:3], 0, v[2:3]
	global_load_dwordx4 v[74:77], v[4:5], off offset:16
	global_load_dwordx4 v[78:81], v[4:5], off
	global_load_dwordx4 v[34:37], v[2:3], off offset:16
	global_load_dwordx4 v[38:41], v[2:3], off
	v_readlane_b32 s2, v255, 53
	v_readlane_b32 s3, v255, 54
	s_andn2_b64 vcc, exec, s[2:3]
	v_readlane_b32 s73, v255, 30
	v_readlane_b32 s74, v255, 31
	v_readlane_b32 s75, v255, 32
	v_readlane_b32 s78, v255, 35
	v_readlane_b32 s79, v255, 36
	v_readlane_b32 s82, v255, 39
	v_readlane_b32 s83, v255, 40
	v_readlane_b32 s84, v255, 41
	v_readlane_b32 s85, v255, 42
	v_readlane_b32 s86, v255, 43
	v_readlane_b32 s87, v255, 44
	s_cbranch_vccnz .LBB0_725
	s_barrier
	s_branch .LBB0_725

; __device__ __forceinline__ float sat8(float x) { return __builtin_amdgcn_fmed3f(x, -448.0f, 448.0f); }
; __device__ __forceinline__ unsigned pk4_fp8(float a, float b, float c, float d) { int v = 0; v = __builtin_amdgcn_cvt_pk_fp8_f32(a, b, v, false); v = __builtin_amdgcn_cvt_pk_fp8_f32(c, d, v, true); return (unsigned)v; }
;     __device__ __forceinline__ void operator()(const f32x4 (&acc)[2][2][4][2], const pg8::Unit& u, const Pre& q, int wr, int wc, int fr, int fq) const {
;         const int rl0 = wr * 64 + fr, colw = u.pn * 256 + wc * 32;
;         constexpr float DS = 1.0f / (FP8_SH * FP8_SW);
; #pragma unroll
;         for (int ai = 0; ai < 2; ++ai)
; #pragma unroll
;             for (int mp = 0; mp < 2; ++mp)
; #pragma unroll
;                 for (int bj = 0; bj < 2; ++bj) { unsigned lo[2], hi[2];
; #pragma unroll
;                     for (int mm = 0; mm < 2; ++mm) { const int m = 2 * mp + mm; const float gt = q.gt[ai][m] * FP8_SY;
;                         const f32x4 v0 = (acc[ai][bj][m][0] * DS + q.bv[bj][0]) * gt, v1 = (acc[ai][bj][m][1] * DS + q.bv[bj][1]) * gt;
;                         lo[mm] = pk4_fp8(sat8(v0[0]), sat8(v0[1]), sat8(v0[2]), sat8(v0[3])); hi[mm] = pk4_fp8(sat8(v1[0]), sat8(v1[1]), sat8(v1[2]), sat8(v1[3])); }
;                     const v2u r0 = __builtin_amdgcn_permlane16_swap(lo[0], lo[1], false, false), r1 = __builtin_amdgcn_permlane16_swap(hi[0], hi[1], false, false);
;                     unsigned char* rowp = y2 + (size_t)(u.pm * 256 + rl0 + ai * 128 + (2 * mp + (fq & 1)) * 16) * D + colw + bj * 128 + 16 * (fq >> 1);
;                     *(v4u*)rowp = (v4u){r0.x, r1.x, r0.y, r1.y}; }
;     }
.LBB0_810:
	v_mov_b32_e32 v3, v0
	s_lshl_b32 s24, s24, 8
	v_readfirstlane_b32 s15, v3
	s_ashr_i32 s17, s15, 2
	s_lshr_b32 s15, s15, 1
	s_and_b32 s15, s15, 0x60
	s_andn2_b32 s17, s17, 63
	s_or_b32 s24, s15, s24
	s_lshl_b32 s15, s22, 8
	s_add_i32 s17, s17, s15
	v_and_or_b32 v2, v3, 31, s17
	v_lshrrev_b32_e32 v3, 1, v3
	s_waitcnt vmcnt(8)
	v_mul_f32_e32 v10, 0x42000000, v197
	v_pk_fma_f32 v[4:5], v[176:177], s[10:11], v[48:49] op_sel_hi:[1,0,1]
	v_pk_fma_f32 v[6:7], v[174:175], s[10:11], v[46:47] op_sel_hi:[1,0,1]
	v_and_b32_e32 v178, 16, v3
	v_ashrrev_i32_e32 v3, 31, v2
	v_pk_mul_f32 v[4:5], v[10:11], v[4:5] op_sel_hi:[0,1]
	v_pk_mul_f32 v[6:7], v[10:11], v[6:7] op_sel_hi:[0,1]
	v_pk_fma_f32 v[14:15], v[170:171], s[10:11], v[42:43] op_sel_hi:[1,0,1]
	v_lshlrev_b64 v[8:9], 11, v[2:3]
	v_pk_fma_f32 v[12:13], v[172:173], s[10:11], v[44:45] op_sel_hi:[1,0,1]
	v_pk_mul_f32 v[14:15], v[10:11], v[14:15] op_sel_hi:[0,1]
	v_med3_f32 v3, v6, s79, v189
	v_med3_f32 v6, v7, s79, v189
	v_med3_f32 v7, v4, s79, v189
	v_mov_b32_e32 v4, v179
	v_pk_mul_f32 v[12:13], v[10:11], v[12:13] op_sel_hi:[0,1]
	v_med3_f32 v11, v5, s79, v189
	v_cvt_pk_fp8_f32 v4, v3, v6
	v_med3_f32 v3, v14, s79, v189
	v_med3_f32 v6, v15, s79, v189
	v_mov_b32_e32 v5, v179
	v_cvt_pk_fp8_f32 v5, v3, v6
	v_med3_f32 v3, v12, s79, v189
	v_med3_f32 v6, v13, s79, v189
	v_cvt_pk_fp8_f32 v4, v7, v11 op_sel:[0,0,1]
	v_cvt_pk_fp8_f32 v5, v3, v6 op_sel:[0,0,1]
	v_mul_f32_e32 v12, 0x42000000, v196
	v_pk_fma_f32 v[6:7], v[168:169], s[10:11], v[48:49] op_sel_hi:[1,0,1]
	v_pk_fma_f32 v[14:15], v[166:167], s[10:11], v[46:47] op_sel_hi:[1,0,1]
	v_pk_mul_f32 v[6:7], v[12:13], v[6:7] op_sel_hi:[0,1]
	v_pk_mul_f32 v[14:15], v[12:13], v[14:15] op_sel_hi:[0,1]
	v_pk_fma_f32 v[16:17], v[164:165], s[10:11], v[44:45] op_sel_hi:[1,0,1]
	v_pk_fma_f32 v[18:19], v[162:163], s[10:11], v[42:43] op_sel_hi:[1,0,1]
	v_pk_mul_f32 v[16:17], v[12:13], v[16:17] op_sel_hi:[0,1]
	v_pk_mul_f32 v[18:19], v[12:13], v[18:19] op_sel_hi:[0,1]
	v_med3_f32 v3, v14, s79, v189
	v_med3_f32 v11, v15, s79, v189
	v_med3_f32 v13, v6, s79, v189
	v_mov_b32_e32 v6, v179
	v_med3_f32 v14, v7, s79, v189
	v_cvt_pk_fp8_f32 v6, v3, v11
	v_med3_f32 v3, v18, s79, v189
	v_med3_f32 v11, v19, s79, v189
	v_mov_b32_e32 v7, v179
	v_cvt_pk_fp8_f32 v7, v3, v11
	v_med3_f32 v3, v16, s79, v189
	v_med3_f32 v11, v17, s79, v189
	v_cvt_pk_fp8_f32 v6, v13, v14 op_sel:[0,0,1]
	v_cvt_pk_fp8_f32 v7, v3, v11 op_sel:[0,0,1]
	s_ashr_i32 s25, s24, 31
	v_lshl_add_u64 v[8:9], s[6:7], 0, v[8:9]
	v_lshl_add_u64 v[8:9], v[8:9], 0, s[24:25]
	v_permlane16_swap_b32_e32 v4, v6
	v_permlane16_swap_b32_e32 v5, v7
	v_lshl_add_u64 v[8:9], v[8:9], 0, v[178:179]
	global_store_dwordx4 v[8:9], v[4:7], off
	s_cmp_lg_u64 s[8:9], 0
	s_cbranch_scc0 .Lalign8
	s_barrier
.Lalign8:
	v_pk_fma_f32 v[14:15], v[156:157], s[10:11], v[36:37] op_sel_hi:[1,0,1]
	v_pk_fma_f32 v[16:17], v[154:155], s[10:11], v[34:35] op_sel_hi:[1,0,1]
	v_pk_fma_f32 v[4:5], v[160:161], s[10:11], v[40:41] op_sel_hi:[1,0,1]
	v_pk_fma_f32 v[6:7], v[158:159], s[10:11], v[38:39] op_sel_hi:[1,0,1]
	v_pk_mul_f32 v[4:5], v[10:11], v[4:5] op_sel_hi:[0,1]
	v_pk_mul_f32 v[6:7], v[10:11], v[6:7] op_sel_hi:[0,1]
	v_pk_mul_f32 v[14:15], v[10:11], v[14:15] op_sel_hi:[0,1]
	v_pk_mul_f32 v[10:11], v[10:11], v[16:17] op_sel_hi:[0,1]
	v_med3_f32 v3, v6, s79, v189
	v_med3_f32 v6, v7, s79, v189
	v_med3_f32 v7, v4, s79, v189
	v_mov_b32_e32 v4, v179
	v_med3_f32 v13, v5, s79, v189
	v_cvt_pk_fp8_f32 v4, v3, v6
	v_med3_f32 v3, v10, s79, v189
	v_med3_f32 v6, v11, s79, v189
	v_mov_b32_e32 v5, v179
	v_cvt_pk_fp8_f32 v5, v3, v6
	v_med3_f32 v3, v14, s79, v189
	v_med3_f32 v6, v15, s79, v189
	v_cvt_pk_fp8_f32 v4, v7, v13 op_sel:[0,0,1]
	v_cvt_pk_fp8_f32 v5, v3, v6 op_sel:[0,0,1]
	v_pk_fma_f32 v[6:7], v[152:153], s[10:11], v[40:41] op_sel_hi:[1,0,1]
	v_pk_fma_f32 v[10:11], v[150:151], s[10:11], v[38:39] op_sel_hi:[1,0,1]
	v_pk_mul_f32 v[6:7], v[12:13], v[6:7] op_sel_hi:[0,1]
	v_pk_mul_f32 v[10:11], v[12:13], v[10:11] op_sel_hi:[0,1]
	v_pk_fma_f32 v[14:15], v[148:149], s[10:11], v[36:37] op_sel_hi:[1,0,1]
	v_pk_fma_f32 v[16:17], v[146:147], s[10:11], v[34:35] op_sel_hi:[1,0,1]
	v_pk_mul_f32 v[14:15], v[12:13], v[14:15] op_sel_hi:[0,1]
	v_pk_mul_f32 v[12:13], v[12:13], v[16:17] op_sel_hi:[0,1]
	v_med3_f32 v3, v10, s79, v189
	v_med3_f32 v10, v11, s79, v189
	v_med3_f32 v11, v6, s79, v189
	v_mov_b32_e32 v6, v179
	v_med3_f32 v16, v7, s79, v189
	v_cvt_pk_fp8_f32 v6, v3, v10
	v_med3_f32 v3, v12, s79, v189
	v_med3_f32 v10, v13, s79, v189
	v_mov_b32_e32 v7, v179
	v_cvt_pk_fp8_f32 v7, v3, v10
	v_med3_f32 v3, v14, s79, v189
	v_med3_f32 v10, v15, s79, v189
	v_cvt_pk_fp8_f32 v6, v11, v16 op_sel:[0,0,1]
	v_cvt_pk_fp8_f32 v7, v3, v10 op_sel:[0,0,1]
	v_mul_f32_e32 v10, 0x42000000, v195
	v_pk_fma_f32 v[14:15], v[138:139], s[10:11], v[42:43] op_sel_hi:[1,0,1]
	v_permlane16_swap_b32_e32 v4, v6
	v_permlane16_swap_b32_e32 v5, v7
	global_store_dwordx4 v[8:9], v[4:7], off offset:128
	v_pk_fma_f32 v[12:13], v[140:141], s[10:11], v[44:45] op_sel_hi:[1,0,1]
	v_pk_mul_f32 v[14:15], v[10:11], v[14:15] op_sel_hi:[0,1]
	v_or_b32_e32 v4, 32, v2
	v_ashrrev_i32_e32 v5, 31, v4
	v_lshlrev_b64 v[8:9], 11, v[4:5]
	v_pk_fma_f32 v[4:5], v[144:145], s[10:11], v[48:49] op_sel_hi:[1,0,1]
	v_pk_fma_f32 v[6:7], v[142:143], s[10:11], v[46:47] op_sel_hi:[1,0,1]
	v_pk_mul_f32 v[4:5], v[10:11], v[4:5] op_sel_hi:[0,1]
	v_pk_mul_f32 v[6:7], v[10:11], v[6:7] op_sel_hi:[0,1]
	v_med3_f32 v3, v6, s79, v189
	v_med3_f32 v6, v7, s79, v189
	v_med3_f32 v7, v4, s79, v189
	v_mov_b32_e32 v4, v179
	v_pk_mul_f32 v[12:13], v[10:11], v[12:13] op_sel_hi:[0,1]
	v_med3_f32 v11, v5, s79, v189
	v_cvt_pk_fp8_f32 v4, v3, v6
; __device__ __forceinline__ float sat8(float x) { return __builtin_amdgcn_fmed3f(x, -448.0f, 448.0f); }
; __device__ __forceinline__ unsigned pk4_fp8(float a, float b, float c, float d) { int v = 0; v = __builtin_amdgcn_cvt_pk_fp8_f32(a, b, v, false); v = __builtin_amdgcn_cvt_pk_fp8_f32(c, d, v, true); return (unsigned)v; }
;     __device__ __forceinline__ void operator()(const f32x4 (&acc)[2][2][4][2], const pg8::Unit& u, const Pre& q, int wr, int wc, int fr, int fq) const {
;     ...
;                 for (int bj = 0; bj < 2; ++bj) { unsigned lo[2], hi[2];
; #pragma unroll
;                     for (int mm = 0; mm < 2; ++mm) { const int m = 2 * mp + mm; const float gt = q.gt[ai][m] * FP8_SY;
;                         const f32x4 v0 = (acc[ai][bj][m][0] * DS + q.bv[bj][0]) * gt, v1 = (acc[ai][bj][m][1] * DS + q.bv[bj][1]) * gt;
;                         lo[mm] = pk4_fp8(sat8(v0[0]), sat8(v0[1]), sat8(v0[2]), sat8(v0[3])); hi[mm] = pk4_fp8(sat8(v1[0]), sat8(v1[1]), sat8(v1[2]), sat8(v1[3])); }
;                     const v2u r0 = __builtin_amdgcn_permlane16_swap(lo[0], lo[1], false, false), r1 = __builtin_amdgcn_permlane16_swap(hi[0], hi[1], false, false);
;                     unsigned char* rowp = y2 + (size_t)(u.pm * 256 + rl0 + ai * 128 + (2 * mp + (fq & 1)) * 16) * D + colw + bj * 128 + 16 * (fq >> 1);
;                     *(v4u*)rowp = (v4u){r0.x, r1.x, r0.y, r1.y}; }
	v_med3_f32 v3, v14, s79, v189
	v_med3_f32 v6, v15, s79, v189
	v_mov_b32_e32 v5, v179
	v_cvt_pk_fp8_f32 v5, v3, v6
	v_med3_f32 v3, v12, s79, v189
	v_med3_f32 v6, v13, s79, v189
	v_cvt_pk_fp8_f32 v4, v7, v11 op_sel:[0,0,1]
	v_cvt_pk_fp8_f32 v5, v3, v6 op_sel:[0,0,1]
	v_mul_f32_e32 v12, 0x42000000, v194
	v_pk_fma_f32 v[6:7], v[136:137], s[10:11], v[48:49] op_sel_hi:[1,0,1]
	v_pk_fma_f32 v[14:15], v[134:135], s[10:11], v[46:47] op_sel_hi:[1,0,1]
	v_pk_mul_f32 v[6:7], v[12:13], v[6:7] op_sel_hi:[0,1]
	v_pk_mul_f32 v[14:15], v[12:13], v[14:15] op_sel_hi:[0,1]
	v_pk_fma_f32 v[16:17], v[132:133], s[10:11], v[44:45] op_sel_hi:[1,0,1]
	v_pk_fma_f32 v[18:19], v[130:131], s[10:11], v[42:43] op_sel_hi:[1,0,1]
	v_pk_mul_f32 v[16:17], v[12:13], v[16:17] op_sel_hi:[0,1]
	v_pk_mul_f32 v[18:19], v[12:13], v[18:19] op_sel_hi:[0,1]
	v_med3_f32 v3, v14, s79, v189
	v_med3_f32 v11, v15, s79, v189
	v_med3_f32 v13, v6, s79, v189
	v_mov_b32_e32 v6, v179
	v_med3_f32 v14, v7, s79, v189
	v_cvt_pk_fp8_f32 v6, v3, v11
	v_med3_f32 v3, v18, s79, v189
	v_med3_f32 v11, v19, s79, v189
	v_mov_b32_e32 v7, v179
	v_cvt_pk_fp8_f32 v7, v3, v11
	v_med3_f32 v3, v16, s79, v189
	v_med3_f32 v11, v17, s79, v189
	v_cvt_pk_fp8_f32 v6, v13, v14 op_sel:[0,0,1]
	v_cvt_pk_fp8_f32 v7, v3, v11 op_sel:[0,0,1]
	v_lshl_add_u64 v[8:9], s[6:7], 0, v[8:9]
	v_lshl_add_u64 v[8:9], v[8:9], 0, s[24:25]
	v_permlane16_swap_b32_e32 v4, v6
	v_permlane16_swap_b32_e32 v5, v7
	v_lshl_add_u64 v[8:9], v[8:9], 0, v[178:179]
	global_store_dwordx4 v[8:9], v[4:7], off
	v_pk_fma_f32 v[14:15], v[124:125], s[10:11], v[36:37] op_sel_hi:[1,0,1]
	v_pk_fma_f32 v[16:17], v[122:123], s[10:11], v[34:35] op_sel_hi:[1,0,1]
	v_pk_fma_f32 v[4:5], v[128:129], s[10:11], v[40:41] op_sel_hi:[1,0,1]
	v_pk_fma_f32 v[6:7], v[126:127], s[10:11], v[38:39] op_sel_hi:[1,0,1]
	v_pk_mul_f32 v[4:5], v[10:11], v[4:5] op_sel_hi:[0,1]
	v_pk_mul_f32 v[6:7], v[10:11], v[6:7] op_sel_hi:[0,1]
	v_pk_mul_f32 v[14:15], v[10:11], v[14:15] op_sel_hi:[0,1]
	v_pk_mul_f32 v[10:11], v[10:11], v[16:17] op_sel_hi:[0,1]
	v_med3_f32 v3, v6, s79, v189
	v_med3_f32 v6, v7, s79, v189
	v_med3_f32 v7, v4, s79, v189
	v_mov_b32_e32 v4, v179
	v_med3_f32 v13, v5, s79, v189
	v_cvt_pk_fp8_f32 v4, v3, v6
	v_med3_f32 v3, v10, s79, v189
	v_med3_f32 v6, v11, s79, v189
	v_mov_b32_e32 v5, v179
	v_cvt_pk_fp8_f32 v5, v3, v6
	v_med3_f32 v3, v14, s79, v189
	v_med3_f32 v6, v15, s79, v189
	v_cvt_pk_fp8_f32 v4, v7, v13 op_sel:[0,0,1]
	v_cvt_pk_fp8_f32 v5, v3, v6 op_sel:[0,0,1]
	v_pk_fma_f32 v[6:7], v[120:121], s[10:11], v[40:41] op_sel_hi:[1,0,1]
	v_pk_fma_f32 v[10:11], v[118:119], s[10:11], v[38:39] op_sel_hi:[1,0,1]
	v_pk_mul_f32 v[6:7], v[12:13], v[6:7] op_sel_hi:[0,1]
	v_pk_mul_f32 v[10:11], v[12:13], v[10:11] op_sel_hi:[0,1]
	v_pk_fma_f32 v[14:15], v[116:117], s[10:11], v[36:37] op_sel_hi:[1,0,1]
	v_pk_fma_f32 v[16:17], v[114:115], s[10:11], v[34:35] op_sel_hi:[1,0,1]
	v_pk_mul_f32 v[14:15], v[12:13], v[14:15] op_sel_hi:[0,1]
	v_pk_mul_f32 v[12:13], v[12:13], v[16:17] op_sel_hi:[0,1]
	v_med3_f32 v3, v10, s79, v189
	v_med3_f32 v10, v11, s79, v189
	v_med3_f32 v11, v6, s79, v189
	v_mov_b32_e32 v6, v179
	v_med3_f32 v16, v7, s79, v189
	v_cvt_pk_fp8_f32 v6, v3, v10
	v_med3_f32 v3, v12, s79, v189
	v_med3_f32 v10, v13, s79, v189
	v_mov_b32_e32 v7, v179
	v_cvt_pk_fp8_f32 v7, v3, v10
	v_med3_f32 v3, v14, s79, v189
	v_med3_f32 v10, v15, s79, v189
	v_cvt_pk_fp8_f32 v6, v11, v16 op_sel:[0,0,1]
	v_cvt_pk_fp8_f32 v7, v3, v10 op_sel:[0,0,1]
	v_mul_f32_e32 v10, 0x42000000, v193
	v_pk_fma_f32 v[14:15], v[106:107], s[10:11], v[42:43] op_sel_hi:[1,0,1]
	v_permlane16_swap_b32_e32 v4, v6
	v_permlane16_swap_b32_e32 v5, v7
	global_store_dwordx4 v[8:9], v[4:7], off offset:128
	v_pk_fma_f32 v[12:13], v[108:109], s[10:11], v[44:45] op_sel_hi:[1,0,1]
	v_pk_mul_f32 v[14:15], v[10:11], v[14:15] op_sel_hi:[0,1]
	v_add_u32_e32 v4, 0x80, v2
	v_ashrrev_i32_e32 v5, 31, v4
	v_lshlrev_b64 v[8:9], 11, v[4:5]
	v_pk_fma_f32 v[4:5], v[112:113], s[10:11], v[48:49] op_sel_hi:[1,0,1]
	v_pk_fma_f32 v[6:7], v[110:111], s[10:11], v[46:47] op_sel_hi:[1,0,1]
	v_pk_mul_f32 v[4:5], v[10:11], v[4:5] op_sel_hi:[0,1]
	v_pk_mul_f32 v[6:7], v[10:11], v[6:7] op_sel_hi:[0,1]
	v_med3_f32 v3, v6, s79, v189
	v_med3_f32 v6, v7, s79, v189
	v_med3_f32 v7, v4, s79, v189
	v_mov_b32_e32 v4, v179
	v_pk_mul_f32 v[12:13], v[10:11], v[12:13] op_sel_hi:[0,1]
	v_med3_f32 v11, v5, s79, v189
	v_cvt_pk_fp8_f32 v4, v3, v6
	v_med3_f32 v3, v14, s79, v189
	v_med3_f32 v6, v15, s79, v189
	v_mov_b32_e32 v5, v179
	v_cvt_pk_fp8_f32 v5, v3, v6
	v_med3_f32 v3, v12, s79, v189
	v_med3_f32 v6, v13, s79, v189
	v_cvt_pk_fp8_f32 v4, v7, v11 op_sel:[0,0,1]
	v_cvt_pk_fp8_f32 v5, v3, v6 op_sel:[0,0,1]
	v_mul_f32_e32 v12, 0x42000000, v192
	v_pk_fma_f32 v[6:7], v[104:105], s[10:11], v[48:49] op_sel_hi:[1,0,1]
	v_pk_fma_f32 v[14:15], v[102:103], s[10:11], v[46:47] op_sel_hi:[1,0,1]
	v_pk_mul_f32 v[6:7], v[12:13], v[6:7] op_sel_hi:[0,1]
	v_pk_mul_f32 v[14:15], v[12:13], v[14:15] op_sel_hi:[0,1]
	v_pk_fma_f32 v[16:17], v[100:101], s[10:11], v[44:45] op_sel_hi:[1,0,1]
	v_pk_fma_f32 v[18:19], v[98:99], s[10:11], v[42:43] op_sel_hi:[1,0,1]
	v_pk_mul_f32 v[16:17], v[12:13], v[16:17] op_sel_hi:[0,1]
	v_pk_mul_f32 v[18:19], v[12:13], v[18:19] op_sel_hi:[0,1]
	v_med3_f32 v3, v14, s79, v189
	v_med3_f32 v11, v15, s79, v189
	v_med3_f32 v13, v6, s79, v189
	v_mov_b32_e32 v6, v179
	v_med3_f32 v14, v7, s79, v189
	v_cvt_pk_fp8_f32 v6, v3, v11
	v_med3_f32 v3, v18, s79, v189
	v_med3_f32 v11, v19, s79, v189
	v_mov_b32_e32 v7, v179
	v_cvt_pk_fp8_f32 v7, v3, v11
	v_med3_f32 v3, v16, s79, v189
	v_med3_f32 v11, v17, s79, v189
	v_cvt_pk_fp8_f32 v6, v13, v14 op_sel:[0,0,1]
	v_cvt_pk_fp8_f32 v7, v3, v11 op_sel:[0,0,1]
; __device__ __forceinline__ float sat8(float x) { return __builtin_amdgcn_fmed3f(x, -448.0f, 448.0f); }
; __device__ __forceinline__ unsigned pk4_fp8(float a, float b, float c, float d) { int v = 0; v = __builtin_amdgcn_cvt_pk_fp8_f32(a, b, v, false); v = __builtin_amdgcn_cvt_pk_fp8_f32(c, d, v, true); return (unsigned)v; }
;     __device__ __forceinline__ void operator()(const f32x4 (&acc)[2][2][4][2], const pg8::Unit& u, const Pre& q, int wr, int wc, int fr, int fq) const {
;     ...
;                 for (int bj = 0; bj < 2; ++bj) { unsigned lo[2], hi[2];
; #pragma unroll
;                     for (int mm = 0; mm < 2; ++mm) { const int m = 2 * mp + mm; const float gt = q.gt[ai][m] * FP8_SY;
;                         const f32x4 v0 = (acc[ai][bj][m][0] * DS + q.bv[bj][0]) * gt, v1 = (acc[ai][bj][m][1] * DS + q.bv[bj][1]) * gt;
;                         lo[mm] = pk4_fp8(sat8(v0[0]), sat8(v0[1]), sat8(v0[2]), sat8(v0[3])); hi[mm] = pk4_fp8(sat8(v1[0]), sat8(v1[1]), sat8(v1[2]), sat8(v1[3])); }
;                     const v2u r0 = __builtin_amdgcn_permlane16_swap(lo[0], lo[1], false, false), r1 = __builtin_amdgcn_permlane16_swap(hi[0], hi[1], false, false);
;                     unsigned char* rowp = y2 + (size_t)(u.pm * 256 + rl0 + ai * 128 + (2 * mp + (fq & 1)) * 16) * D + colw + bj * 128 + 16 * (fq >> 1);
;                     *(v4u*)rowp = (v4u){r0.x, r1.x, r0.y, r1.y}; }
	v_lshl_add_u64 v[8:9], s[6:7], 0, v[8:9]
	v_lshl_add_u64 v[8:9], v[8:9], 0, s[24:25]
	v_permlane16_swap_b32_e32 v4, v6
	v_permlane16_swap_b32_e32 v5, v7
	v_lshl_add_u64 v[8:9], v[8:9], 0, v[178:179]
	global_store_dwordx4 v[8:9], v[4:7], off
	v_pk_fma_f32 v[14:15], v[92:93], s[10:11], v[36:37] op_sel_hi:[1,0,1]
	v_pk_fma_f32 v[16:17], v[90:91], s[10:11], v[34:35] op_sel_hi:[1,0,1]
	v_pk_fma_f32 v[4:5], v[96:97], s[10:11], v[40:41] op_sel_hi:[1,0,1]
	v_pk_fma_f32 v[6:7], v[94:95], s[10:11], v[38:39] op_sel_hi:[1,0,1]
	v_pk_mul_f32 v[4:5], v[10:11], v[4:5] op_sel_hi:[0,1]
	v_pk_mul_f32 v[6:7], v[10:11], v[6:7] op_sel_hi:[0,1]
	v_pk_mul_f32 v[14:15], v[10:11], v[14:15] op_sel_hi:[0,1]
	v_pk_mul_f32 v[10:11], v[10:11], v[16:17] op_sel_hi:[0,1]
	v_med3_f32 v3, v6, s79, v189
	v_med3_f32 v6, v7, s79, v189
	v_med3_f32 v7, v4, s79, v189
	v_mov_b32_e32 v4, v179
	v_med3_f32 v13, v5, s79, v189
	v_cvt_pk_fp8_f32 v4, v3, v6
	v_med3_f32 v3, v10, s79, v189
	v_med3_f32 v6, v11, s79, v189
	v_mov_b32_e32 v5, v179
	v_cvt_pk_fp8_f32 v5, v3, v6
	v_med3_f32 v3, v14, s79, v189
	v_med3_f32 v6, v15, s79, v189
	v_cvt_pk_fp8_f32 v4, v7, v13 op_sel:[0,0,1]
	v_cvt_pk_fp8_f32 v5, v3, v6 op_sel:[0,0,1]
	v_pk_fma_f32 v[6:7], v[88:89], s[10:11], v[40:41] op_sel_hi:[1,0,1]
	v_pk_fma_f32 v[10:11], v[86:87], s[10:11], v[38:39] op_sel_hi:[1,0,1]
	v_pk_mul_f32 v[6:7], v[12:13], v[6:7] op_sel_hi:[0,1]
	v_pk_mul_f32 v[10:11], v[12:13], v[10:11] op_sel_hi:[0,1]
	v_pk_fma_f32 v[14:15], v[84:85], s[10:11], v[36:37] op_sel_hi:[1,0,1]
	v_pk_fma_f32 v[16:17], v[82:83], s[10:11], v[34:35] op_sel_hi:[1,0,1]
	v_pk_mul_f32 v[14:15], v[12:13], v[14:15] op_sel_hi:[0,1]
	v_pk_mul_f32 v[12:13], v[12:13], v[16:17] op_sel_hi:[0,1]
	v_med3_f32 v3, v10, s79, v189
	v_med3_f32 v10, v11, s79, v189
	v_med3_f32 v11, v6, s79, v189
	v_mov_b32_e32 v6, v179
	v_med3_f32 v16, v7, s79, v189
	v_cvt_pk_fp8_f32 v6, v3, v10
	v_med3_f32 v3, v12, s79, v189
	v_med3_f32 v10, v13, s79, v189
	v_mov_b32_e32 v7, v179
	v_cvt_pk_fp8_f32 v7, v3, v10
	v_med3_f32 v3, v14, s79, v189
	v_med3_f32 v10, v15, s79, v189
	v_cvt_pk_fp8_f32 v6, v11, v16 op_sel:[0,0,1]
	v_cvt_pk_fp8_f32 v7, v3, v10 op_sel:[0,0,1]
	v_add_u32_e32 v2, 0xa0, v2
	v_ashrrev_i32_e32 v3, 31, v2
	v_permlane16_swap_b32_e32 v4, v6
	v_permlane16_swap_b32_e32 v5, v7
	global_store_dwordx4 v[8:9], v[4:7], off offset:128
	v_mul_f32_e32 v8, 0x42000000, v191
	v_pk_fma_f32 v[10:11], v[76:77], s[10:11], v[44:45] op_sel_hi:[1,0,1]
	v_lshlrev_b64 v[6:7], 11, v[2:3]
	v_pk_fma_f32 v[2:3], v[80:81], s[10:11], v[48:49] op_sel_hi:[1,0,1]
	v_pk_fma_f32 v[4:5], v[78:79], s[10:11], v[46:47] op_sel_hi:[1,0,1]
	v_pk_mul_f32 v[2:3], v[8:9], v[2:3] op_sel_hi:[0,1]
	v_pk_mul_f32 v[4:5], v[8:9], v[4:5] op_sel_hi:[0,1]
	v_pk_fma_f32 v[12:13], v[74:75], s[10:11], v[42:43] op_sel_hi:[1,0,1]
	v_pk_mul_f32 v[10:11], v[8:9], v[10:11] op_sel_hi:[0,1]
	v_pk_mul_f32 v[12:13], v[8:9], v[12:13] op_sel_hi:[0,1]
	v_med3_f32 v4, v4, s79, v189
	v_med3_f32 v5, v5, s79, v189
	v_med3_f32 v9, v2, s79, v189
	v_mov_b32_e32 v2, v179
	v_med3_f32 v14, v3, s79, v189
	v_cvt_pk_fp8_f32 v2, v4, v5
	v_med3_f32 v4, v12, s79, v189
	v_med3_f32 v5, v13, s79, v189
	v_mov_b32_e32 v3, v179
	v_cvt_pk_fp8_f32 v3, v4, v5
	v_med3_f32 v4, v10, s79, v189
	v_med3_f32 v5, v11, s79, v189
	v_mul_f32_e32 v10, 0x42000000, v190
	v_cvt_pk_fp8_f32 v3, v4, v5 op_sel:[0,0,1]
	v_pk_fma_f32 v[4:5], v[72:73], s[10:11], v[48:49] op_sel_hi:[1,0,1]
	v_pk_fma_f32 v[12:13], v[70:71], s[10:11], v[46:47] op_sel_hi:[1,0,1]
	v_cvt_pk_fp8_f32 v2, v9, v14 op_sel:[0,0,1]
	v_pk_mul_f32 v[4:5], v[10:11], v[4:5] op_sel_hi:[0,1]
	v_pk_mul_f32 v[12:13], v[10:11], v[12:13] op_sel_hi:[0,1]
	v_pk_fma_f32 v[14:15], v[68:69], s[10:11], v[44:45] op_sel_hi:[1,0,1]
	v_pk_fma_f32 v[16:17], v[66:67], s[10:11], v[42:43] op_sel_hi:[1,0,1]
	v_pk_mul_f32 v[14:15], v[10:11], v[14:15] op_sel_hi:[0,1]
	v_pk_mul_f32 v[16:17], v[10:11], v[16:17] op_sel_hi:[0,1]
	v_med3_f32 v9, v12, s79, v189
	v_med3_f32 v11, v13, s79, v189
	v_med3_f32 v12, v4, s79, v189
	v_mov_b32_e32 v4, v179
	v_med3_f32 v13, v5, s79, v189
	v_cvt_pk_fp8_f32 v4, v9, v11
	v_med3_f32 v9, v16, s79, v189
	v_med3_f32 v11, v17, s79, v189
	v_mov_b32_e32 v5, v179
	v_cvt_pk_fp8_f32 v5, v9, v11
	v_med3_f32 v9, v14, s79, v189
	v_med3_f32 v11, v15, s79, v189
	v_cvt_pk_fp8_f32 v4, v12, v13 op_sel:[0,0,1]
	v_cvt_pk_fp8_f32 v5, v9, v11 op_sel:[0,0,1]
	v_lshl_add_u64 v[6:7], s[6:7], 0, v[6:7]
	v_lshl_add_u64 v[6:7], v[6:7], 0, s[24:25]
	v_permlane16_swap_b32_e32 v2, v4
	v_permlane16_swap_b32_e32 v3, v5
	v_lshl_add_u64 v[6:7], v[6:7], 0, v[178:179]
	global_store_dwordx4 v[6:7], v[2:5], off
	v_pk_fma_f32 v[12:13], v[60:61], s[10:11], v[36:37] op_sel_hi:[1,0,1]
	v_pk_fma_f32 v[14:15], v[58:59], s[10:11], v[34:35] op_sel_hi:[1,0,1]
	v_pk_fma_f32 v[2:3], v[64:65], s[10:11], v[40:41] op_sel_hi:[1,0,1]
	v_pk_fma_f32 v[4:5], v[62:63], s[10:11], v[38:39] op_sel_hi:[1,0,1]
	v_pk_mul_f32 v[2:3], v[8:9], v[2:3] op_sel_hi:[0,1]
	v_pk_mul_f32 v[4:5], v[8:9], v[4:5] op_sel_hi:[0,1]
	v_pk_mul_f32 v[12:13], v[8:9], v[12:13] op_sel_hi:[0,1]
	v_pk_mul_f32 v[8:9], v[8:9], v[14:15] op_sel_hi:[0,1]
	v_med3_f32 v4, v4, s79, v189
	v_med3_f32 v5, v5, s79, v189
	v_med3_f32 v11, v2, s79, v189
	v_mov_b32_e32 v2, v179
	v_med3_f32 v14, v3, s79, v189
	v_cvt_pk_fp8_f32 v2, v4, v5
	v_med3_f32 v4, v8, s79, v189
	v_med3_f32 v5, v9, s79, v189
	v_mov_b32_e32 v3, v179
	v_cvt_pk_fp8_f32 v3, v4, v5
	v_med3_f32 v4, v12, s79, v189
	v_med3_f32 v5, v13, s79, v189
	v_pk_fma_f32 v[8:9], v[54:55], s[10:11], v[38:39] op_sel_hi:[1,0,1]
	v_cvt_pk_fp8_f32 v3, v4, v5 op_sel:[0,0,1]
	v_pk_fma_f32 v[4:5], v[56:57], s[10:11], v[40:41] op_sel_hi:[1,0,1]
	v_cvt_pk_fp8_f32 v2, v11, v14 op_sel:[0,0,1]
	v_pk_mul_f32 v[4:5], v[10:11], v[4:5] op_sel_hi:[0,1]
	v_pk_mul_f32 v[8:9], v[10:11], v[8:9] op_sel_hi:[0,1]
	v_pk_fma_f32 v[12:13], v[52:53], s[10:11], v[36:37] op_sel_hi:[1,0,1]
	v_pk_fma_f32 v[14:15], v[50:51], s[10:11], v[34:35] op_sel_hi:[1,0,1]
	v_pk_mul_f32 v[12:13], v[10:11], v[12:13] op_sel_hi:[0,1]
	v_pk_mul_f32 v[10:11], v[10:11], v[14:15] op_sel_hi:[0,1]
	v_med3_f32 v8, v8, s79, v189
	v_med3_f32 v9, v9, s79, v189
	v_med3_f32 v14, v4, s79, v189
	v_mov_b32_e32 v4, v179
	v_med3_f32 v15, v5, s79, v189
	v_cvt_pk_fp8_f32 v4, v8, v9
	v_med3_f32 v8, v10, s79, v189
	v_med3_f32 v9, v11, s79, v189
	v_mov_b32_e32 v5, v179
	v_cvt_pk_fp8_f32 v5, v8, v9
	v_med3_f32 v8, v12, s79, v189
	v_med3_f32 v9, v13, s79, v189
	v_cvt_pk_fp8_f32 v4, v14, v15 op_sel:[0,0,1]
	v_cvt_pk_fp8_f32 v5, v8, v9 op_sel:[0,0,1]
	s_andn2_b64 vcc, exec, s[0:1]
	s_mov_b64 s[0:1], -1
	v_permlane16_swap_b32_e32 v2, v4
	v_permlane16_swap_b32_e32 v3, v5
	v_readlane_b32 s38, v255, 28
	global_store_dwordx4 v[6:7], v[2:5], off offset:128
	s_cbranch_vccnz .LBB0_803
; #define PG8_BAR __builtin_amdgcn_s_barrier()
; template <class Epi, class Sched>
; __device__ __forceinline__ void gemm_phase(LAS unsigned char* lds, const Sched& S, const Epi& E) {
;     ...
;         cur = nxt; cA = nA; cB = nB; crot = nrot; ++ui;
;         E.prefetch(cur, epre);
;         if (wr == 1) PG8_BAR;
;     __device__ __forceinline__ void prefetch(const pg8::Unit& u, Pre& q) const {
;         int tz = threadIdx.x; asm volatile("" : "+v"(tz)); const int wid = tz >> 6, wr = wid >> 2, wc = wid & 3, fr = tz & 15, fq = (tz >> 4) & 3;
;         const int rl0 = wr * 64 + fr, col0 = u.pn * 256 + wc * 32 + 8 * fq;
;         const int mt = __builtin_amdgcn_readfirstlane(u.pm - tstart[u.e]);
;         const float* gp = sgate + (size_t)u.e * T + mt * 256;
; #pragma unroll
;         for (int bj = 0; bj < 2; ++bj)
; #pragma unroll
;             for (int n = 0; n < 2; ++n) q.bv[bj][n] = *(const f32x4*)(b_down + (size_t)u.e * D + col0 + bj * 128 + 4 * n);
; #pragma unroll
;         for (int ai = 0; ai < 2; ++ai)
; #pragma unroll
;             for (int m = 0; m < 4; ++m) q.gt[ai][m] = gp[rl0 + ai * 128 + m * 16];
;     }
	s_lshl_b32 s0, s96, 2
	s_add_i32 s0, s0, 0
	s_add_i32 s0, s0, 0x27d00
	v_mov_b32_e32 v4, v0
	v_mov_b32_e32 v2, s0
	ds_read_b32 v3, v2
	v_lshrrev_b32_e32 v2, 1, v4
	s_ashr_i32 s97, s96, 31
	v_readlane_b32 s16, v255, 29
	v_and_b32_e32 v2, 0x78, v2
	s_waitcnt lgkmcnt(0)
	v_sub_u32_e32 v3, s14, v3
	s_lshl_b64 s[0:1], s[96:97], 17
	v_readfirstlane_b32 s15, v3
	s_lshl_b32 s34, s15, 8
	s_ashr_i32 s35, s34, 31
	s_lshl_b64 s[36:37], s[96:97], 13
	v_readlane_b32 s26, v255, 39
	v_readlane_b32 s28, v255, 41
	v_lshl_or_b32 v2, s12, 8, v2
	v_readlane_b32 s27, v255, 40
	v_readlane_b32 s29, v255, 42
	s_add_u32 s26, s28, s36
	v_ashrrev_i32_e32 v3, 31, v2
	s_addc_u32 s27, s29, s37
	v_readlane_b32 s17, v255, 30
	v_lshl_add_u64 v[2:3], v[2:3], 2, s[26:27]
	s_add_u32 s15, s11, s0
	v_ashrrev_i32_e32 v5, 2, v4
	global_load_dwordx4 v[42:45], v[2:3], off offset:16
	global_load_dwordx4 v[46:49], v[2:3], off
	global_load_dwordx4 v[34:37], v[2:3], off offset:528
	global_load_dwordx4 v[38:41], v[2:3], off offset:512
	v_and_b32_e32 v2, 15, v4
	s_addc_u32 s17, s42, s1
	s_lshl_b64 s[0:1], s[34:35], 2
	v_and_or_b32 v2, v5, s91, v2
	s_add_u32 s0, s15, s0
	s_addc_u32 s1, s17, s1
	v_ashrrev_i32_e32 v3, 31, v2
	v_lshl_add_u64 v[2:3], v[2:3], 2, s[0:1]
	global_load_dword v197, v[2:3], off
	global_load_dword v196, v[2:3], off offset:64
	global_load_dword v195, v[2:3], off offset:128
	global_load_dword v194, v[2:3], off offset:192
	global_load_dword v193, v[2:3], off offset:512
	global_load_dword v192, v[2:3], off offset:576
	global_load_dword v191, v[2:3], off offset:640
	global_load_dword v190, v[2:3], off offset:704
	s_andn2_b64 vcc, exec, s[4:5]
	v_readlane_b32 s18, v255, 31
	v_readlane_b32 s19, v255, 32
	v_readlane_b32 s20, v255, 33
	v_readlane_b32 s21, v255, 34
	v_readlane_b32 s22, v255, 35
	v_readlane_b32 s23, v255, 36
	v_readlane_b32 s24, v255, 37
	v_readlane_b32 s25, v255, 38
	v_readlane_b32 s30, v255, 43
	v_readlane_b32 s31, v255, 44
	s_cbranch_vccnz .LBB0_802
	s_barrier
	s_branch .LBB0_802
